# barrier poll compacted: 16 XCD generation flags packed in one 64-byte line (4 dwordx4 polls), arrival test by flag sum >= nx*(gen+1)
# speedup vs baseline: 1.0006x; 1.0006x over previous
; __device__ __forceinline__ unsigned xb_ld(unsigned* p)              { return __hip_atomic_load(p, __ATOMIC_RELAXED, __HIP_MEMORY_SCOPE_AGENT); }
; __device__ __forceinline__ unsigned xb_add(unsigned* p, unsigned v) { return __hip_atomic_fetch_add(p, v, __ATOMIC_RELAXED, __HIP_MEMORY_SCOPE_AGENT); }
; #define XB_SPIN(cond, bar) do { unsigned _sp = 0; while (cond) { __builtin_amdgcn_s_sleep(1); \
;     if ((++_sp & 255u) == 0u) { if (xb_ld(&(bar)[XB_TMO])) break; if (_sp > XB_SPIN_CAP) { atomicAdd(&(bar)[XB_TMO], 1u); break; } } } } while (0)
; __device__ __forceinline__ void xcd_barrier(const XcdBarrier& b) {
;     ...
;         unsigned nloc = b.st[0], nx = b.st[1];
;         if (nloc == 0u) { xcd_barrier_complete(bar, b.x, nloc, nx); b.st[0] = nloc; b.st[1] = nx; }
;         const unsigned old = xb_add(&bar[XB_XSUB(b.x)], one_);
;         const unsigned gen = old / nloc;
;         if (old + 1u == (gen + 1u) * nloc) {
;             __builtin_amdgcn_fence(__ATOMIC_RELEASE, "agent");
;             asm volatile("s_waitcnt vmcnt(0)" ::: "memory");
;             const unsigned og = xb_add(&bar[XB_TOP], one_);
;             const unsigned tg = og / nx;
;             if (og + 1u == (tg + 1u) * nx) xb_add(&bar[XB_TOPGEN], one_);
;             else XB_SPIN(xb_ld(&bar[XB_TOPGEN]) == tg, bar);
;             __builtin_amdgcn_fence(__ATOMIC_ACQUIRE, "agent");
;             xb_add(&bar[XB_XGEN(b.x)], one_);
;             asm volatile("s_waitcnt vmcnt(0)" ::: "memory");
;         } else {
;             XB_SPIN(xb_ld(&bar[XB_XGEN(b.x)]) == gen, bar);
;             __builtin_amdgcn_fence(__ATOMIC_ACQUIRE, "agent");
;             asm volatile("s_waitcnt vmcnt(0)" ::: "memory");
;         }
.LBB0_142:
	s_lshl_b32 s2, s33, 8
	s_add_u32 s23, s34, s2
	s_addc_u32 s22, s35, 0
	v_mov_b32_e32 v1, s23
	v_add_co_u32_e32 v4, vcc, 0x1000, v1
	v_mov_b32_e32 v1, s22
	s_nop 0
	v_addc_co_u32_e32 v5, vcc, 0, v1, vcc
	flat_atomic_add v1, v[4:5], v10 offset:1024 sc0
	v_cvt_f32_u32_e32 v3, v2
	v_sub_u32_e32 v4, 0, v2
	v_rcp_iflag_f32_e32 v3, v3
	s_nop 0
	v_mul_f32_e32 v3, 0x4f7ffffe, v3
	v_cvt_u32_f32_e32 v3, v3
	v_mul_lo_u32 v4, v4, v3
	v_mul_hi_u32 v4, v3, v4
	v_add_u32_e32 v3, v3, v4
	s_waitcnt vmcnt(0) lgkmcnt(0)
	v_mul_hi_u32 v3, v1, v3
	v_mul_lo_u32 v5, v3, v2
	v_add_u32_e32 v4, 1, v1
	v_sub_u32_e32 v1, v1, v5
	v_add_u32_e32 v6, 1, v3
	v_cmp_ge_u32_e32 vcc, v1, v2
	v_sub_u32_e32 v5, v1, v2
	s_nop 0
	v_cndmask_b32_e32 v3, v3, v6, vcc
	v_cndmask_b32_e32 v1, v1, v5, vcc
	v_add_u32_e32 v5, 1, v3
	v_cmp_ge_u32_e32 vcc, v1, v2
	s_nop 1
	v_cndmask_b32_e32 v1, v3, v5, vcc
	v_mad_u64_u32 v[2:3], s[2:3], v2, v1, v[2:3]
	v_cmp_ne_u32_e32 vcc, v4, v2
	v_mov_b32_e32 v20, 0
	s_cbranch_vccnz .Lxbar0_poll
	buffer_wbl2 sc1
	s_waitcnt vmcnt(0)
	s_sub_u32 s2, s23, s34
	s_lshr_b32 s2, s2, 6
	s_add_u32 s6, s34, 0x2400
	s_addc_u32 s7, s35, 0
	s_add_u32 s6, s6, s2
	s_addc_u32 s7, s7, 0
	global_atomic_add v20, v10, s[6:7]
.Lxbar0_poll:
	buffer_inv sc1
	s_add_u32 s6, s34, 0x2400
	s_addc_u32 s7, s35, 0
	v_add_u32_e32 v1, 1, v1
	v_mul_lo_u32 v1, v1, v0
	s_mov_b32 s2, 0
.Lxbar0_spin:
	global_load_dwordx4 v[4:7], v20, s[6:7] sc1
	global_load_dwordx4 v[8:11], v20, s[6:7] offset:16 sc1
	global_load_dwordx4 v[12:15], v20, s[6:7] offset:32 sc1
	global_load_dwordx4 v[16:19], v20, s[6:7] offset:48 sc1
	s_waitcnt vmcnt(0)
	v_add3_u32 v2, v4, v5, v6
	v_add3_u32 v2, v2, v7, v8
	v_add3_u32 v2, v2, v9, v10
	v_add3_u32 v2, v2, v11, v12
	v_add3_u32 v2, v2, v13, v14
	v_add3_u32 v2, v2, v15, v16
	v_add3_u32 v2, v2, v17, v18
	v_add_u32_e32 v2, v2, v19
	v_cmp_ge_u32_e32 vcc, v2, v1
	s_cbranch_vccnz .Lxbar0_done
	s_sleep 1
	s_add_i32 s2, s2, 1
	s_cmp_lt_u32 s2, 0x80000
	s_cbranch_scc1 .Lxbar0_spin

; __device__ __forceinline__ unsigned xb_ld(unsigned* p)              { return __hip_atomic_load(p, __ATOMIC_RELAXED, __HIP_MEMORY_SCOPE_AGENT); }
; __device__ __forceinline__ unsigned xb_add(unsigned* p, unsigned v) { return __hip_atomic_fetch_add(p, v, __ATOMIC_RELAXED, __HIP_MEMORY_SCOPE_AGENT); }
; #define XB_SPIN(cond, bar) do { unsigned _sp = 0; while (cond) { __builtin_amdgcn_s_sleep(1); \
;     if ((++_sp & 255u) == 0u) { if (xb_ld(&(bar)[XB_TMO])) break; if (_sp > XB_SPIN_CAP) { atomicAdd(&(bar)[XB_TMO], 1u); break; } } } } while (0)
; __device__ __forceinline__ void xcd_barrier(const XcdBarrier& b) {
;     ...
;         unsigned nloc = b.st[0], nx = b.st[1];
;         if (nloc == 0u) { xcd_barrier_complete(bar, b.x, nloc, nx); b.st[0] = nloc; b.st[1] = nx; }
;         const unsigned old = xb_add(&bar[XB_XSUB(b.x)], one_);
;         const unsigned gen = old / nloc;
;         if (old + 1u == (gen + 1u) * nloc) {
;             __builtin_amdgcn_fence(__ATOMIC_RELEASE, "agent");
;             asm volatile("s_waitcnt vmcnt(0)" ::: "memory");
;             const unsigned og = xb_add(&bar[XB_TOP], one_);
;             const unsigned tg = og / nx;
;             if (og + 1u == (tg + 1u) * nx) xb_add(&bar[XB_TOPGEN], one_);
;             else XB_SPIN(xb_ld(&bar[XB_TOPGEN]) == tg, bar);
;             __builtin_amdgcn_fence(__ATOMIC_ACQUIRE, "agent");
;             xb_add(&bar[XB_XGEN(b.x)], one_);
;             asm volatile("s_waitcnt vmcnt(0)" ::: "memory");
;         } else {
;             XB_SPIN(xb_ld(&bar[XB_XGEN(b.x)]) == gen, bar);
;             __builtin_amdgcn_fence(__ATOMIC_ACQUIRE, "agent");
;             asm volatile("s_waitcnt vmcnt(0)" ::: "memory");
;         }
.LBB0_430:
	v_readlane_b32 s4, v253, 57
	s_lshl_b32 s4, s4, 2
	s_add_u32 s25, s2, s4
	s_addc_u32 s24, s3, 0
	v_mov_b32_e32 v3, s25
	v_add_co_u32_e32 v6, vcc, 0x1000, v3
	v_mov_b32_e32 v3, s24
	s_nop 0
	v_addc_co_u32_e32 v7, vcc, 0, v3, vcc
	flat_atomic_add v5, v[6:7], v1 offset:1024 sc0
	v_cvt_f32_u32_e32 v3, v4
	v_sub_u32_e32 v6, 0, v4
	v_rcp_iflag_f32_e32 v3, v3
	s_nop 0
	v_mul_f32_e32 v3, 0x4f7ffffe, v3
	v_cvt_u32_f32_e32 v3, v3
	v_mul_lo_u32 v6, v6, v3
	v_mul_hi_u32 v6, v3, v6
	v_add_u32_e32 v3, v3, v6
	s_waitcnt vmcnt(0) lgkmcnt(0)
	v_mul_hi_u32 v3, v5, v3
	v_mul_lo_u32 v6, v3, v4
	v_sub_u32_e32 v6, v5, v6
	v_cmp_ge_u32_e32 vcc, v6, v4
	v_add_u32_e32 v7, 1, v3
	s_nop 0
	v_cndmask_b32_e32 v3, v3, v7, vcc
	v_sub_u32_e32 v7, v6, v4
	v_cndmask_b32_e32 v6, v6, v7, vcc
	v_cmp_ge_u32_e32 vcc, v6, v4
	v_add_u32_e32 v6, 1, v3
	s_nop 0
	v_cndmask_b32_e32 v3, v3, v6, vcc
	v_add_u32_e32 v6, 1, v5
	v_mad_u64_u32 v[4:5], s[4:5], v4, v3, v[4:5]
	v_cmp_ne_u32_e32 vcc, v6, v4
	v_mov_b32_e32 v20, 0
	s_cbranch_vccnz .Lxbar1_poll
	buffer_wbl2 sc1
	s_waitcnt vmcnt(0)
	s_sub_u32 s4, s25, s2
	s_lshr_b32 s4, s4, 6
	s_add_u32 s8, s2, 0x2400
	s_addc_u32 s9, s3, 0
	s_add_u32 s8, s8, s4
	s_addc_u32 s9, s9, 0
	global_atomic_add v20, v1, s[8:9]
.Lxbar1_poll:
	buffer_inv sc1
	s_add_u32 s8, s2, 0x2400
	s_addc_u32 s9, s3, 0
	v_add_u32_e32 v3, 1, v3
	v_mul_lo_u32 v3, v3, v0
	s_mov_b32 s4, 0
.Lxbar1_spin:
	global_load_dwordx4 v[4:7], v20, s[8:9] sc1
	global_load_dwordx4 v[8:11], v20, s[8:9] offset:16 sc1
	global_load_dwordx4 v[12:15], v20, s[8:9] offset:32 sc1
	global_load_dwordx4 v[16:19], v20, s[8:9] offset:48 sc1
	s_waitcnt vmcnt(0)
	v_add3_u32 v1, v4, v5, v6
	v_add3_u32 v1, v1, v7, v8
	v_add3_u32 v1, v1, v9, v10
	v_add3_u32 v1, v1, v11, v12
	v_add3_u32 v1, v1, v13, v14
	v_add3_u32 v1, v1, v15, v16
	v_add3_u32 v1, v1, v17, v18
	v_add_u32_e32 v1, v1, v19
	v_cmp_ge_u32_e32 vcc, v1, v3
	s_cbranch_vccnz .Lxbar1_done
	s_sleep 1
	s_add_i32 s4, s4, 1
	s_cmp_lt_u32 s4, 0x80000
	s_cbranch_scc1 .Lxbar1_spin

; __device__ __forceinline__ unsigned xb_ld(unsigned* p)              { return __hip_atomic_load(p, __ATOMIC_RELAXED, __HIP_MEMORY_SCOPE_AGENT); }
; __device__ __forceinline__ unsigned xb_add(unsigned* p, unsigned v) { return __hip_atomic_fetch_add(p, v, __ATOMIC_RELAXED, __HIP_MEMORY_SCOPE_AGENT); }
; #define XB_SPIN(cond, bar) do { unsigned _sp = 0; while (cond) { __builtin_amdgcn_s_sleep(1); \
;     if ((++_sp & 255u) == 0u) { if (xb_ld(&(bar)[XB_TMO])) break; if (_sp > XB_SPIN_CAP) { atomicAdd(&(bar)[XB_TMO], 1u); break; } } } } while (0)
; __device__ __forceinline__ void xcd_barrier(const XcdBarrier& b) {
;     ...
;         unsigned nloc = b.st[0], nx = b.st[1];
;         if (nloc == 0u) { xcd_barrier_complete(bar, b.x, nloc, nx); b.st[0] = nloc; b.st[1] = nx; }
;         const unsigned old = xb_add(&bar[XB_XSUB(b.x)], one_);
;         const unsigned gen = old / nloc;
;         if (old + 1u == (gen + 1u) * nloc) {
;             __builtin_amdgcn_fence(__ATOMIC_RELEASE, "agent");
;             asm volatile("s_waitcnt vmcnt(0)" ::: "memory");
;             const unsigned og = xb_add(&bar[XB_TOP], one_);
;             const unsigned tg = og / nx;
;             if (og + 1u == (tg + 1u) * nx) xb_add(&bar[XB_TOPGEN], one_);
;             else XB_SPIN(xb_ld(&bar[XB_TOPGEN]) == tg, bar);
;             __builtin_amdgcn_fence(__ATOMIC_ACQUIRE, "agent");
;             xb_add(&bar[XB_XGEN(b.x)], one_);
;             asm volatile("s_waitcnt vmcnt(0)" ::: "memory");
;         } else {
;             XB_SPIN(xb_ld(&bar[XB_XGEN(b.x)]) == gen, bar);
;             __builtin_amdgcn_fence(__ATOMIC_ACQUIRE, "agent");
;             asm volatile("s_waitcnt vmcnt(0)" ::: "memory");
;         }
.LBB0_681:
	v_readlane_b32 s6, v253, 57
	s_lshl_b32 s6, s6, 2
	s_add_u32 s27, s4, s6
	s_addc_u32 s26, s5, 0
	v_mov_b32_e32 v3, s27
	v_add_co_u32_e32 v6, vcc, 0x1000, v3
	v_mov_b32_e32 v3, s26
	s_nop 0
	v_addc_co_u32_e32 v7, vcc, 0, v3, vcc
	flat_atomic_add v5, v[6:7], v1 offset:1024 sc0
	v_cvt_f32_u32_e32 v3, v4
	v_sub_u32_e32 v6, 0, v4
	v_rcp_iflag_f32_e32 v3, v3
	s_nop 0
	v_mul_f32_e32 v3, 0x4f7ffffe, v3
	v_cvt_u32_f32_e32 v3, v3
	v_mul_lo_u32 v6, v6, v3
	v_mul_hi_u32 v6, v3, v6
	v_add_u32_e32 v3, v3, v6
	s_waitcnt vmcnt(0) lgkmcnt(0)
	v_mul_hi_u32 v3, v5, v3
	v_mul_lo_u32 v6, v3, v4
	v_sub_u32_e32 v6, v5, v6
	v_cmp_ge_u32_e32 vcc, v6, v4
	v_add_u32_e32 v7, 1, v3
	s_nop 0
	v_cndmask_b32_e32 v3, v3, v7, vcc
	v_sub_u32_e32 v7, v6, v4
	v_cndmask_b32_e32 v6, v6, v7, vcc
	v_cmp_ge_u32_e32 vcc, v6, v4
	v_add_u32_e32 v6, 1, v3
	s_nop 0
	v_cndmask_b32_e32 v3, v3, v6, vcc
	v_add_u32_e32 v6, 1, v5
	v_mad_u64_u32 v[4:5], s[6:7], v4, v3, v[4:5]
	v_cmp_ne_u32_e32 vcc, v6, v4
	v_mov_b32_e32 v20, 0
	s_cbranch_vccnz .Lxbar2_poll
	buffer_wbl2 sc1
	s_waitcnt vmcnt(0)
	s_sub_u32 s6, s27, s4
	s_lshr_b32 s6, s6, 6
	s_add_u32 s10, s4, 0x2400
	s_addc_u32 s11, s5, 0
	s_add_u32 s10, s10, s6
	s_addc_u32 s11, s11, 0
	global_atomic_add v20, v1, s[10:11]
.Lxbar2_poll:
	buffer_inv sc1
	s_add_u32 s10, s4, 0x2400
	s_addc_u32 s11, s5, 0
	v_add_u32_e32 v3, 1, v3
	v_mul_lo_u32 v3, v3, v0
	s_mov_b32 s6, 0
.Lxbar2_spin:
	global_load_dwordx4 v[4:7], v20, s[10:11] sc1
	global_load_dwordx4 v[8:11], v20, s[10:11] offset:16 sc1
	global_load_dwordx4 v[12:15], v20, s[10:11] offset:32 sc1
	global_load_dwordx4 v[16:19], v20, s[10:11] offset:48 sc1
	s_waitcnt vmcnt(0)
	v_add3_u32 v1, v4, v5, v6
	v_add3_u32 v1, v1, v7, v8
	v_add3_u32 v1, v1, v9, v10
	v_add3_u32 v1, v1, v11, v12
	v_add3_u32 v1, v1, v13, v14
	v_add3_u32 v1, v1, v15, v16
	v_add3_u32 v1, v1, v17, v18
	v_add_u32_e32 v1, v1, v19
	v_cmp_ge_u32_e32 vcc, v1, v3
	s_cbranch_vccnz .Lxbar2_done
	s_sleep 1
	s_add_i32 s6, s6, 1
	s_cmp_lt_u32 s6, 0x80000
	s_cbranch_scc1 .Lxbar2_spin

; __device__ __forceinline__ unsigned xb_ld(unsigned* p)              { return __hip_atomic_load(p, __ATOMIC_RELAXED, __HIP_MEMORY_SCOPE_AGENT); }
; __device__ __forceinline__ unsigned xb_add(unsigned* p, unsigned v) { return __hip_atomic_fetch_add(p, v, __ATOMIC_RELAXED, __HIP_MEMORY_SCOPE_AGENT); }
; #define XB_SPIN(cond, bar) do { unsigned _sp = 0; while (cond) { __builtin_amdgcn_s_sleep(1); \
;     if ((++_sp & 255u) == 0u) { if (xb_ld(&(bar)[XB_TMO])) break; if (_sp > XB_SPIN_CAP) { atomicAdd(&(bar)[XB_TMO], 1u); break; } } } } while (0)
; __device__ __forceinline__ void xcd_barrier(const XcdBarrier& b) {
;     ...
;         unsigned nloc = b.st[0], nx = b.st[1];
;         if (nloc == 0u) { xcd_barrier_complete(bar, b.x, nloc, nx); b.st[0] = nloc; b.st[1] = nx; }
;         const unsigned old = xb_add(&bar[XB_XSUB(b.x)], one_);
;         const unsigned gen = old / nloc;
;         if (old + 1u == (gen + 1u) * nloc) {
;             __builtin_amdgcn_fence(__ATOMIC_RELEASE, "agent");
;             asm volatile("s_waitcnt vmcnt(0)" ::: "memory");
;             const unsigned og = xb_add(&bar[XB_TOP], one_);
;             const unsigned tg = og / nx;
;             if (og + 1u == (tg + 1u) * nx) xb_add(&bar[XB_TOPGEN], one_);
;             else XB_SPIN(xb_ld(&bar[XB_TOPGEN]) == tg, bar);
;             __builtin_amdgcn_fence(__ATOMIC_ACQUIRE, "agent");
;             xb_add(&bar[XB_XGEN(b.x)], one_);
.LBB0_928:
	v_readlane_b32 s6, v253, 57
	s_lshl_b32 s6, s6, 2
	s_add_u32 s29, s4, s6
	s_addc_u32 s28, s5, 0
	v_mov_b32_e32 v3, s29
	v_add_co_u32_e32 v6, vcc, 0x1000, v3
	v_mov_b32_e32 v3, s28
	s_nop 0
	v_addc_co_u32_e32 v7, vcc, 0, v3, vcc
	flat_atomic_add v5, v[6:7], v1 offset:1024 sc0
	v_cvt_f32_u32_e32 v3, v4
	v_sub_u32_e32 v6, 0, v4
	v_rcp_iflag_f32_e32 v3, v3
	s_nop 0
	v_mul_f32_e32 v3, 0x4f7ffffe, v3
	v_cvt_u32_f32_e32 v3, v3
	v_mul_lo_u32 v6, v6, v3
	v_mul_hi_u32 v6, v3, v6
	v_add_u32_e32 v3, v3, v6
	s_waitcnt vmcnt(0) lgkmcnt(0)
	v_mul_hi_u32 v3, v5, v3
	v_mul_lo_u32 v6, v3, v4
	v_sub_u32_e32 v6, v5, v6
	v_cmp_ge_u32_e32 vcc, v6, v4
	v_add_u32_e32 v7, 1, v3
	s_nop 0
	v_cndmask_b32_e32 v3, v3, v7, vcc
	v_sub_u32_e32 v7, v6, v4
	v_cndmask_b32_e32 v6, v6, v7, vcc
	v_cmp_ge_u32_e32 vcc, v6, v4
	v_add_u32_e32 v6, 1, v3
	s_nop 0
	v_cndmask_b32_e32 v3, v3, v6, vcc
	v_add_u32_e32 v6, 1, v5
	v_mad_u64_u32 v[4:5], s[6:7], v4, v3, v[4:5]
	v_cmp_ne_u32_e32 vcc, v6, v4
	v_mov_b32_e32 v20, 0
	s_cbranch_vccnz .Lxbar4_poll
	buffer_wbl2 sc1
	s_waitcnt vmcnt(0)
	s_sub_u32 s6, s29, s4
	s_lshr_b32 s6, s6, 6
	s_add_u32 s10, s4, 0x2400
	s_addc_u32 s11, s5, 0
	s_add_u32 s10, s10, s6
	s_addc_u32 s11, s11, 0
	global_atomic_add v20, v1, s[10:11]

; __device__ __forceinline__ unsigned xb_ld(unsigned* p)              { return __hip_atomic_load(p, __ATOMIC_RELAXED, __HIP_MEMORY_SCOPE_AGENT); }
; __device__ __forceinline__ unsigned xb_add(unsigned* p, unsigned v) { return __hip_atomic_fetch_add(p, v, __ATOMIC_RELAXED, __HIP_MEMORY_SCOPE_AGENT); }
; #define XB_SPIN(cond, bar) do { unsigned _sp = 0; while (cond) { __builtin_amdgcn_s_sleep(1); \
;     if ((++_sp & 255u) == 0u) { if (xb_ld(&(bar)[XB_TMO])) break; if (_sp > XB_SPIN_CAP) { atomicAdd(&(bar)[XB_TMO], 1u); break; } } } } while (0)
; __device__ __forceinline__ void xcd_barrier(const XcdBarrier& b) {
;     ...
;         unsigned nloc = b.st[0], nx = b.st[1];
;         if (nloc == 0u) { xcd_barrier_complete(bar, b.x, nloc, nx); b.st[0] = nloc; b.st[1] = nx; }
;         const unsigned old = xb_add(&bar[XB_XSUB(b.x)], one_);
;         const unsigned gen = old / nloc;
;         if (old + 1u == (gen + 1u) * nloc) {
;             __builtin_amdgcn_fence(__ATOMIC_RELEASE, "agent");
;             asm volatile("s_waitcnt vmcnt(0)" ::: "memory");
;             const unsigned og = xb_add(&bar[XB_TOP], one_);
;             const unsigned tg = og / nx;
;             if (og + 1u == (tg + 1u) * nx) xb_add(&bar[XB_TOPGEN], one_);
;             else XB_SPIN(xb_ld(&bar[XB_TOPGEN]) == tg, bar);
;             __builtin_amdgcn_fence(__ATOMIC_ACQUIRE, "agent");
;             xb_add(&bar[XB_XGEN(b.x)], one_);
.LBB0_1016:
	v_readlane_b32 s4, v253, 57
	s_lshl_b32 s4, s4, 2
	s_add_u32 s27, s2, s4
	s_addc_u32 s26, s3, 0
	v_mov_b32_e32 v3, s27
	v_add_co_u32_e32 v6, vcc, 0x1000, v3
	v_mov_b32_e32 v3, s26
	s_nop 0
	v_addc_co_u32_e32 v7, vcc, 0, v3, vcc
	flat_atomic_add v5, v[6:7], v1 offset:1024 sc0
	v_cvt_f32_u32_e32 v3, v4
	v_sub_u32_e32 v6, 0, v4
	v_rcp_iflag_f32_e32 v3, v3
	s_nop 0
	v_mul_f32_e32 v3, 0x4f7ffffe, v3
	v_cvt_u32_f32_e32 v3, v3
	v_mul_lo_u32 v6, v6, v3
	v_mul_hi_u32 v6, v3, v6
	v_add_u32_e32 v3, v3, v6
	s_waitcnt vmcnt(0) lgkmcnt(0)
	v_mul_hi_u32 v3, v5, v3
	v_mul_lo_u32 v6, v3, v4
	v_sub_u32_e32 v6, v5, v6
	v_cmp_ge_u32_e32 vcc, v6, v4
	v_add_u32_e32 v7, 1, v3
	s_nop 0
	v_cndmask_b32_e32 v3, v3, v7, vcc
	v_sub_u32_e32 v7, v6, v4
	v_cndmask_b32_e32 v6, v6, v7, vcc
	v_cmp_ge_u32_e32 vcc, v6, v4
	v_add_u32_e32 v6, 1, v3
	s_nop 0
	v_cndmask_b32_e32 v3, v3, v6, vcc
	v_add_u32_e32 v6, 1, v5
	v_mad_u64_u32 v[4:5], s[4:5], v4, v3, v[4:5]
	v_cmp_ne_u32_e32 vcc, v6, v4
	v_mov_b32_e32 v20, 0
	s_cbranch_vccnz .Lxbar5_poll
	buffer_wbl2 sc1
	s_waitcnt vmcnt(0)
	s_sub_u32 s4, s27, s2
	s_lshr_b32 s4, s4, 6
	s_add_u32 s8, s2, 0x2400
	s_addc_u32 s9, s3, 0
	s_add_u32 s8, s8, s4
	s_addc_u32 s9, s9, 0
	global_atomic_add v20, v1, s[8:9]
